# speedup vs baseline: 1.0157x; 1.0157x over previous
.Lmk_agg_join:
	s_cmp_lt_i32 s30, 33
	s_cbranch_scc1 .Lmk_st_done
	s_cmp_lt_i32 s66, 33
	s_cbranch_scc1 .Lmk_up_only
	v_mfma_f32_16x16x32_f16 v[54:57], v[146:149], v[160:163], v[54:57]
	ds_write_b128 v196, v[2:5] offset:4096
	v_mfma_f32_16x16x32_f16 v[58:61], v[150:153], v[160:163], v[58:61]
	ds_write_b128 v196, v[6:9] offset:5120
	v_mfma_f32_16x16x32_f16 v[62:65], v[154:157], v[160:163], v[62:65]
	ds_write_b128 v196, v[18:21] offset:6144
	v_mfma_f32_16x16x32_f16 v[66:69], v[204:207], v[160:163], v[66:69]
	ds_write_b128 v196, v[22:25] offset:7168
	v_mfma_f32_16x16x32_f16 v[70:73], v[168:171], v[160:163], v[70:73]

.Lmk_st_done:
	s_cmp_lt_i32 s66, 33
	s_cbranch_scc1 .LBB2_76
	v_mfma_f32_16x16x32_f16 v[54:57], v[146:149], v[160:163], v[54:57]
	v_mfma_f32_16x16x32_f16 v[58:61], v[150:153], v[160:163], v[58:61]
	v_mfma_f32_16x16x32_f16 v[62:65], v[154:157], v[160:163], v[62:65]
	v_mfma_f32_16x16x32_f16 v[66:69], v[204:207], v[160:163], v[66:69]
	v_mfma_f32_16x16x32_f16 v[70:73], v[168:171], v[160:163], v[70:73]
	s_branch .LBB2_76
.Lmk_up_only:
	ds_write_b128 v196, v[2:5] offset:4096
	ds_write_b128 v196, v[6:9] offset:5120
	ds_write_b128 v196, v[18:21] offset:6144
	ds_write_b128 v196, v[22:25] offset:7168
	s_branch .LBB2_76
